# attention K-tile LDS swizzle widened to 4 bits (conflict-free ds_read_b128 of K fragments)
# speedup vs baseline: 1.0146x; 1.0146x over previous
.LBB0_1578:
	s_or_b64 exec, exec, s[26:27]
	v_ashrrev_i32_e32 v44, 3, v109
	v_ashrrev_i32_e32 v45, 31, v44
	v_lshl_add_u64 v[6:7], s[42:43], 0, v[44:45]
	v_lshlrev_b32_e32 v5, 3, v109
	v_lshlrev_b64 v[6:7], 11, v[6:7]
	v_and_b32_e32 v10, 56, v5
	v_lshl_add_u64 v[6:7], s[8:9], 0, v[6:7]
	v_lshl_add_u64 v[6:7], v[40:41], 1, v[6:7]
	v_lshlrev_b32_e32 v80, 1, v10
	v_mov_b32_e32 v81, v3
	v_lshl_add_u64 v[8:9], v[6:7], 0, v[80:81]
	v_lshlrev_b32_e32 v43, 8, v4
	v_and_b32_e32 v4, 0xf0, v109
	v_bitop3_b32 v143, v2, v43, v4 bitop3:0xde
	global_load_dwordx4 v[4:7], v[8:9], off offset:128
	s_movk_i32 s19, 0xf0
	s_waitcnt vmcnt(0)
	v_bitop3_b32 v50, v2, v109, s19 bitop3:0x78
	v_add_u32_e32 v51, 0, v143
	v_add3_u32 v11, v43, v50, 0
	s_and_saveexec_b64 s[26:27], s[40:41]
	s_cbranch_execz .LBB0_1580
	v_lshlrev_b32_e32 v2, 7, v42
	s_waitcnt vmcnt(2)
	ds_write_b128 v51, v[68:71]
	s_waitcnt vmcnt(1)
	ds_write_b128 v11, v[72:75] offset:8192
	v_lshl_add_u64 v[12:13], v[82:83], 0, v[2:3]
	v_mov_b32_e32 v49, v3
	v_lshl_add_u64 v[14:15], v[12:13], 0, v[48:49]
	global_load_dwordx4 v[68:71], v[12:13], off
	global_load_dwordx4 v[72:75], v[14:15], off

.LBB0_1582:
	s_or_b64 exec, exec, s[26:27]
	v_lshl_add_u64 v[46:47], v[8:9], 0, s[24:25]
	v_add_co_u32_e32 v4, vcc, 0x20000, v46
	v_and_b32_e32 v81, 31, v109
	v_bfe_u32 v136, v109, 5, 1
	v_addc_co_u32_e32 v5, vcc, 0, v47, vcc
	global_load_dwordx4 v[36:39], v[4:5], off
	v_lshlrev_b32_e32 v137, 4, v136
	v_lshlrev_b32_e32 v146, 8, v81
	v_lshlrev_b32_e32 v4, 4, v109
	v_add_u32_e32 v152, 0, v146
	v_bitop3_b32 v153, v137, v4, s19 bitop3:0x78
	s_waitcnt lgkmcnt(0)
	s_barrier
	v_add_u32_e32 v150, v152, v153
	v_and_b32_e32 v49, 0xf0, v4
	ds_read_b128 v[4:7], v150
	ds_read_b128 v[8:11], v150 offset:8192
	s_waitcnt lgkmcnt(1)
	v_mfma_f32_32x32x16_bf16 v[20:35], v[4:7], v[100:103], 0
	v_bitop3_b32 v155, v137, v49, 32 bitop3:0x36
	v_add_u32_e32 v154, v152, v155
	ds_read_b128 v[52:55], v154
	ds_read_b128 v[56:59], v154 offset:8192
	v_bitop3_b32 v156, v137, v49, 64 bitop3:0x36
	v_add_u32_e32 v149, v152, v156
	s_movk_i32 s19, 0x60
	v_bitop3_b32 v157, v137, v49, s19 bitop3:0x36
	s_waitcnt lgkmcnt(2)
	v_mfma_f32_32x32x16_bf16 v[4:19], v[8:11], v[100:103], 0
	v_add_u32_e32 v147, v152, v157
	s_movk_i32 s19, 0x80
	v_bitop3_b32 v158, v137, v49, s19 bitop3:0x36
	v_add_u32_e32 v148, v152, v158
	s_movk_i32 s19, 0xa0
	v_bitop3_b32 v159, v137, v49, s19 bitop3:0x36
	v_add_u32_e32 v151, v152, v159
	s_waitcnt lgkmcnt(1)
	v_mfma_f32_32x32x16_bf16 v[20:35], v[52:55], v[96:99], v[20:35]
	v_add_u32_e32 v160, v43, v50
	s_waitcnt lgkmcnt(0)
	v_mfma_f32_32x32x16_bf16 v[4:19], v[56:59], v[96:99], v[4:19]
	ds_read_b128 v[52:55], v149
	ds_read_b128 v[56:59], v149 offset:8192
	s_waitcnt lgkmcnt(1)
	v_mfma_f32_32x32x16_bf16 v[20:35], v[52:55], v[104:107], v[20:35]
	s_waitcnt lgkmcnt(0)
	v_mfma_f32_32x32x16_bf16 v[4:19], v[56:59], v[104:107], v[4:19]
	ds_read_b128 v[52:55], v147
	ds_read_b128 v[56:59], v147 offset:8192
	s_waitcnt lgkmcnt(1)
	v_mfma_f32_32x32x16_bf16 v[20:35], v[52:55], v[92:95], v[20:35]
	s_waitcnt lgkmcnt(0)
	v_mfma_f32_32x32x16_bf16 v[4:19], v[56:59], v[92:95], v[4:19]
	ds_read_b128 v[52:55], v148
	ds_read_b128 v[56:59], v148 offset:8192
	s_waitcnt lgkmcnt(1)
	v_mfma_f32_32x32x16_bf16 v[20:35], v[52:55], v[88:91], v[20:35]
	s_waitcnt lgkmcnt(0)
	v_mfma_f32_32x32x16_bf16 v[4:19], v[56:59], v[88:91], v[4:19]
	ds_read_b128 v[52:55], v151
	ds_read_b128 v[56:59], v151 offset:8192
	s_waitcnt lgkmcnt(1)
	v_mfma_f32_32x32x16_bf16 v[20:35], v[52:55], v[84:87], v[20:35]
	s_waitcnt lgkmcnt(0)
	v_mfma_f32_32x32x16_bf16 v[4:19], v[56:59], v[84:87], v[4:19]
	s_nop 9
	v_max_f32_e32 v49, v21, v21
	v_max_f32_e32 v52, v20, v20
	v_max_f32_e32 v49, v52, v49
	v_max3_f32 v49, v49, v22, v23
	v_max3_f32 v49, v49, v24, v25
	v_max3_f32 v49, v49, v26, v27
	v_max3_f32 v49, v49, v28, v29
	v_max3_f32 v49, v49, v30, v31
	v_max3_f32 v49, v49, v32, v33
	v_max3_f32 v49, v49, v34, v35
	v_max3_f32 v49, v49, v4, v5
	v_max3_f32 v49, v49, v6, v7
	v_max3_f32 v49, v49, v8, v9
	v_max3_f32 v49, v49, v10, v11
	v_max3_f32 v49, v49, v12, v13
	v_max3_f32 v49, v49, v14, v15
	v_max3_f32 v49, v49, v16, v17
	v_max3_f32 v49, v49, v18, v19
	v_mov_b32_e32 v52, v49
	s_nop 1
	v_permlane32_swap_b32_e32 v49, v52
	v_max_f32_e32 v52, v52, v52
	v_max_f32_e32 v49, v49, v49
	v_max_f32_e32 v52, v49, v52
	v_add_f32_e32 v49, 0x7149f2ca, v52
	v_cmp_ge_f32_e32 vcc, s78, v49
	s_cmp_eq_u64 vcc, exec
	s_cselect_b64 vcc, -1, 0
	s_and_saveexec_b64 s[20:21], s[2:3]
	s_xor_b64 s[2:3], exec, s[20:21]
	v_add_u32_e32 v160, v43, v50
	s_andn2_saveexec_b64 s[2:3], s[2:3]
	s_cbranch_execz .LBB0_1586
	v_add_u32_e32 v43, 0, v160
	s_movk_i32 s19, 0x180
	s_waitcnt vmcnt(2)
	ds_write_b128 v51, v[68:71] offset:32768
	s_waitcnt vmcnt(1)
	ds_write_b128 v43, v[72:75] offset:40960
	v_mad_u64_u32 v[50:51], s[20:21], v42, s19, v[82:83]
	v_mov_b32_e32 v49, v3
	v_lshl_add_u64 v[48:49], v[50:51], 0, v[48:49]
	global_load_dwordx4 v[68:71], v[50:51], off
	global_load_dwordx4 v[72:75], v[48:49], off

.LBB0_1621:
	s_or_b64 exec, exec, s[26:27]
	v_ashrrev_i32_e32 v28, 3, v150
	v_ashrrev_i32_e32 v29, 31, v28
	v_lshl_add_u64 v[6:7], s[42:43], 0, v[28:29]
	v_lshlrev_b32_e32 v5, 3, v150
	v_lshlrev_b64 v[6:7], 11, v[6:7]
	v_and_b32_e32 v10, 56, v5
	v_lshl_add_u64 v[6:7], s[8:9], 0, v[6:7]
	v_lshl_add_u64 v[6:7], v[24:25], 1, v[6:7]
	v_lshlrev_b32_e32 v136, 1, v10
	v_mov_b32_e32 v137, v3
	v_lshl_add_u64 v[8:9], v[6:7], 0, v[136:137]
	v_lshlrev_b32_e32 v27, 8, v4
	v_and_b32_e32 v4, 0xf0, v150
	v_bitop3_b32 v154, v2, v27, v4 bitop3:0xde
	global_load_dwordx4 v[4:7], v[8:9], off offset:128
	s_movk_i32 s19, 0xf0
	s_waitcnt vmcnt(0)
	v_bitop3_b32 v34, v2, v150, s19 bitop3:0x78
	v_add_u32_e32 v35, 0, v154
	v_add3_u32 v11, v27, v34, 0
	s_and_saveexec_b64 s[26:27], s[38:39]
	s_cbranch_execz .LBB0_1623
	v_lshlrev_b32_e32 v2, 7, v26
	s_waitcnt vmcnt(2)
	ds_write_b128 v35, v[108:111]
	s_waitcnt vmcnt(1)
	ds_write_b128 v11, v[112:115] offset:8192
	v_lshl_add_u64 v[12:13], v[138:139], 0, v[2:3]
	v_mov_b32_e32 v31, v3
	v_lshl_add_u64 v[14:15], v[12:13], 0, v[30:31]
	global_load_dwordx4 v[108:111], v[12:13], off
	global_load_dwordx4 v[112:115], v[14:15], off

.LBB0_1625:
	s_or_b64 exec, exec, s[26:27]
	v_lshl_add_u64 v[32:33], v[8:9], 0, s[24:25]
	v_and_b32_e32 v137, 31, v150
	v_bfe_u32 v151, v150, 5, 1
	v_add_co_u32_e32 v4, vcc, 0x20000, v32
	v_lshlrev_b32_e32 v153, 4, v151
	v_lshlrev_b32_e32 v162, 8, v137
	v_lshlrev_b32_e32 v31, 4, v150
	v_addc_co_u32_e32 v5, vcc, 0, v33, vcc
	v_add_u32_e32 v164, 0, v162
	v_bitop3_b32 v165, v153, v31, s19 bitop3:0x78
	global_load_dwordx4 v[20:23], v[4:5], off
	s_waitcnt lgkmcnt(0)
	s_barrier
	v_add_u32_e32 v158, v164, v165
	ds_read_b128 v[4:7], v158
	ds_read_b128 v[36:39], v158 offset:8192
	v_and_b32_e32 v31, 0xf0, v31
	v_bitop3_b32 v166, v153, v31, 32 bitop3:0x36
	v_add_u32_e32 v163, v164, v166
	ds_read_b128 v[52:55], v163
	s_waitcnt lgkmcnt(2)
	v_mfma_f32_32x32x16_bf16 v[4:19], v[4:7], v[100:103], 0
	v_bitop3_b32 v167, v153, v31, 64 bitop3:0x36
	v_add_u32_e32 v159, v164, v167
	s_movk_i32 s19, 0x60
	v_bitop3_b32 v168, v153, v31, s19 bitop3:0x36
	v_add_u32_e32 v160, v164, v168
	s_movk_i32 s19, 0x80
	v_bitop3_b32 v169, v153, v31, s19 bitop3:0x36
	s_waitcnt lgkmcnt(0)
	v_mfma_f32_32x32x16_bf16 v[4:19], v[52:55], v[96:99], v[4:19]
	ds_read_b128 v[52:55], v163 offset:8192
	v_add_u32_e32 v161, v164, v169
	s_movk_i32 s19, 0xa0
	v_bitop3_b32 v170, v153, v31, s19 bitop3:0x36
	v_add_u32_e32 v157, v164, v170
	v_add_u32_e32 v171, v27, v34
	v_mfma_f32_32x32x16_bf16 v[36:51], v[36:39], v[100:103], 0
	s_waitcnt lgkmcnt(0)
	v_mfma_f32_32x32x16_bf16 v[36:51], v[52:55], v[96:99], v[36:51]
	ds_read_b128 v[52:55], v159
	s_waitcnt lgkmcnt(0)
	v_mfma_f32_32x32x16_bf16 v[4:19], v[52:55], v[104:107], v[4:19]
	ds_read_b128 v[52:55], v159 offset:8192
	s_waitcnt lgkmcnt(0)
	v_mfma_f32_32x32x16_bf16 v[36:51], v[52:55], v[104:107], v[36:51]
	ds_read_b128 v[52:55], v160
	s_waitcnt lgkmcnt(0)
	v_mfma_f32_32x32x16_bf16 v[4:19], v[52:55], v[92:95], v[4:19]
	ds_read_b128 v[52:55], v160 offset:8192
	s_waitcnt lgkmcnt(0)
	v_mfma_f32_32x32x16_bf16 v[36:51], v[52:55], v[92:95], v[36:51]
	ds_read_b128 v[52:55], v161
	s_waitcnt lgkmcnt(0)
	v_mfma_f32_32x32x16_bf16 v[4:19], v[52:55], v[88:91], v[4:19]
	ds_read_b128 v[52:55], v161 offset:8192
	s_waitcnt lgkmcnt(0)
	v_mfma_f32_32x32x16_bf16 v[36:51], v[52:55], v[88:91], v[36:51]
	ds_read_b128 v[52:55], v157
	s_waitcnt lgkmcnt(0)
	v_mfma_f32_32x32x16_bf16 v[4:19], v[52:55], v[84:87], v[4:19]
	ds_read_b128 v[52:55], v157 offset:8192
	s_waitcnt lgkmcnt(0)
	v_mfma_f32_32x32x16_bf16 v[36:51], v[52:55], v[84:87], v[36:51]
	s_and_saveexec_b64 s[20:21], s[2:3]
	s_xor_b64 s[2:3], exec, s[20:21]
	v_add_u32_e32 v171, v27, v34
	s_andn2_saveexec_b64 s[2:3], s[2:3]
	s_cbranch_execz .LBB0_1629
	v_add_u32_e32 v27, 0, v171
	s_movk_i32 s19, 0x180
	s_waitcnt vmcnt(2)
	ds_write_b128 v35, v[108:111] offset:32768
	s_waitcnt vmcnt(1)
	ds_write_b128 v27, v[112:115] offset:40960
	v_mad_u64_u32 v[34:35], s[20:21], v26, s19, v[138:139]
	v_mov_b32_e32 v31, v3
	v_lshl_add_u64 v[30:31], v[34:35], 0, v[30:31]
	global_load_dwordx4 v[108:111], v[34:35], off
	global_load_dwordx4 v[112:115], v[30:31], off
.LBB0_1629:
	s_or_b64 exec, exec, s[2:3]
	s_mov_b32 s2, 0x40000
	s_nop 1
	v_exp_f32_e32 v174, v4
	v_add_co_u32_e32 v4, vcc, s2, v32
	v_exp_f32_e32 v176, v5
	s_nop 0
	v_addc_co_u32_e32 v5, vcc, 0, v33, vcc
	global_load_dwordx4 v[116:119], v[4:5], off
	v_and_b32_e32 v152, 63, v150
	v_lshlrev_b32_e32 v5, 4, v152
	v_exp_f32_e32 v178, v6
	v_lshlrev_b32_e32 v4, 3, v152
	v_and_b32_e32 v5, 0xc0, v5
	v_lshlrev_b32_e32 v6, 1, v152
	v_and_or_b32 v5, v4, 24, v5
	v_and_b32_e32 v6, 32, v6
	v_and_b32_e32 v4, 0x100, v4
	v_or3_b32 v155, v5, v6, v4
	s_waitcnt vmcnt(1)
	ds_write_b128 v156, v[20:23] offset:57344
	v_bitop3_b32 v4, v151, v150, 15 bitop3:0x78
	s_waitcnt lgkmcnt(0)
	s_barrier
	v_and_b32_e32 v6, 15, v150
	v_lshl_add_u32 v4, v4, 4, v164
	ds_read_b128 v[52:55], v4 offset:16384
	ds_read_b128 v[56:59], v4 offset:24576
	v_bitop3_b32 v4, v151, v6, 2 bitop3:0x36
	v_lshl_add_u32 v4, v4, 4, v164
	ds_read_b128 v[132:135], v4 offset:16384
	ds_read_b128 v[124:127], v4 offset:24576
	v_bitop3_b32 v4, v151, v6, 4 bitop3:0x36
	v_and_b32_e32 v6, 7, v6
	v_lshl_add_u32 v4, v4, 4, v164
	ds_read_b128 v[128:131], v4 offset:16384
	ds_read_b128 v[120:123], v4 offset:24576
	s_lshl_b64 s[20:21], s[36:37], 23
	v_lshlrev_b64 v[4:5], 11, v[28:29]
	v_exp_f32_e32 v180, v7
	v_exp_f32_e32 v182, v8
	v_exp_f32_e32 v184, v9
	v_exp_f32_e32 v186, v10
	v_exp_f32_e32 v187, v11
	v_exp_f32_e32 v175, v12
	v_exp_f32_e32 v177, v13
	v_exp_f32_e32 v179, v14
	v_exp_f32_e32 v181, v15
	v_exp_f32_e32 v183, v16
	v_exp_f32_e32 v185, v17
	v_exp_f32_e32 v188, v18
	v_exp_f32_e32 v189, v19
	v_lshl_add_u64 v[4:5], s[20:21], 0, v[4:5]
	v_lshl_or_b32 v4, v6, 4, v4
	v_lshl_add_u64 v[4:5], v[24:25], 1, v[4:5]
	v_mov_b32_e32 v173, 0
	s_mov_b32 s2, 1
	s_mov_b32 s34, 0
	s_mov_b32 s40, 2
	v_add_u32_e32 v172, 0, v155
	v_mul_hi_u32_u24_e32 v141, 0x2c0, v26
	v_mul_u32_u24_e32 v140, 0x2c0, v26
	v_mul_hi_u32_u24_e32 v143, 0x280, v26
	v_mul_u32_u24_e32 v142, 0x280, v26
	v_mul_hi_u32_u24_e32 v145, 0x240, v26
	v_mul_u32_u24_e32 v144, 0x240, v26
	v_lshlrev_b32_e32 v146, 9, v26
	v_mov_b32_e32 v147, v3
	v_lshl_add_u64 v[148:149], s[14:15], 0, v[4:5]
	s_mov_b32 s3, 0
	s_mov_b32 s41, 1
	s_mov_b32 s43, 2
	s_mov_b32 s42, 1
	v_mov_b32_e32 v4, 0
	v_mov_b32_e32 v5, v173
	v_mov_b32_e32 v6, v173
	v_mov_b32_e32 v7, v173
	v_mov_b32_e32 v8, v173
	v_mov_b32_e32 v9, v173
	v_mov_b32_e32 v10, v173
	v_mov_b32_e32 v11, v173
	v_mov_b32_e32 v12, v173
	v_mov_b32_e32 v13, v173
	v_mov_b32_e32 v14, v173
	v_mov_b32_e32 v15, v173
	v_mov_b32_e32 v16, v173
	v_mov_b32_e32 v17, v173
	v_mov_b32_e32 v18, v173
	v_mov_b32_e32 v19, v173
	v_mov_b32_e32 v20, 0
	v_mov_b32_e32 v21, v173
	v_mov_b32_e32 v22, v173
	v_mov_b32_e32 v23, v173
	v_mov_b32_e32 v24, v173
	v_mov_b32_e32 v25, v173
	v_mov_b32_e32 v26, v173
	v_mov_b32_e32 v27, v173
	v_mov_b32_e32 v28, v173
	v_mov_b32_e32 v29, v173
	v_mov_b32_e32 v30, v173
	v_mov_b32_e32 v31, v173
	v_mov_b32_e32 v32, v173
	v_mov_b32_e32 v33, v173
	v_mov_b32_e32 v34, v173
	v_mov_b32_e32 v35, v173
